# mlstm_D unit start: K-tile and query-fragment requests issued before the gate/normaliser-state loads and the row-max scan (two cold round trips overlapped)
# baseline (speedup 1.0000x reference)
; #define LAS __attribute__((address_space(3)))
; __device__ __forceinline__ int fresh_tid() { int t = threadIdx.x; asm volatile("" : "+v"(t)); return t; }
; __device__ __forceinline__ void mlstm_D(LAS unsigned char* lds, int c, int h, const bf16_t* Z, const float* gi, const float* bcum, const float* marr, const bf16_t* CST, const float* NST,
;                                         const float* hgain, bf16_t* YCAT) {
;     ...
;     const int tid = fresh_tid(), lane = tid & 63, wave = __builtin_amdgcn_readfirstlane(tid >> 6), fr = lane & 15, fq = lane >> 4;
;     LAS unsigned char* X = lds + XOFF; LAS unsigned char* Pw = lds + POFF + wave * 16 * PRS;
;     LAS float* gS = (LAS float*)(lds + SOFF); LAS float* Mrow = gS + CH; LAS float* nst = Mrow + CH;
;     const int t0 = c * CH; const float mc = marr[h * 65 + c];
;     __syncthreads();
;     if (tid < CH) gS[tid] = gi[(size_t)(t0 + tid) * 4 + h];
;     else if (tid < CH + DH) nst[tid - CH] = NST[(size_t)(c * NH + h) * DH + (tid - CH)];
;     __syncthreads();
;     if (tid < CH) { float m = mc; for (int s = 0; s <= tid; ++s) m = fmaxf(m, gS[s]); Mrow[tid] = m; }
;     stage_tile<CH, DH, 8>(X, Z + (size_t)t0 * EVN + 2048 + h * DH, EVN, tid);
;     const int tl = 16 * wave + fr; const size_t trow = (size_t)(t0 + tl);
;     bf16x8 aq[8];
; #pragma unroll
;     for (int ks = 0; ks < 8; ++ks) aq[ks] = *(const bf16x8*)(Z + trow * EVN + 1024 + h * DH + 32 * ks + 8 * fq);
.LBB0_558:
	s_and_b32 s36, s22, 3
	s_ashr_i32 s8, s22, 2
	s_mul_i32 s2, s36, 0x41
	s_add_i32 s2, s2, s8
	s_ashr_i32 s3, s2, 31
	s_lshl_b64 s[2:3], s[2:3], 2
	s_add_u32 s2, s54, s2
	v_mov_b32_e32 v99, v0
	s_addc_u32 s3, s55, s3
	global_load_dword v95, v67, s[2:3]
	v_readfirstlane_b32 s15, v99
	s_lshl_b32 s14, s8, 7
	s_ashr_i32 s23, s15, 6
	s_mul_i32 s3, s14, 0x2800
	s_mul_hi_i32 s2, s14, 0x2800
	s_add_u32 s37, s30, s3
	v_add_u32_e32 v118, 0x200, v99
	s_addc_u32 s66, s31, s2
	s_lshl_b32 s24, s36, 9
	v_ashrrev_i32_e32 v122, 31, v99
	v_ashrrev_i32_e32 v124, 31, v118
	s_add_u32 s2, s37, s24
	v_lshrrev_b32_e32 v2, 27, v122
	v_lshrrev_b32_e32 v4, 27, v124
	s_addc_u32 s3, s66, 0
	v_add_u32_e32 v2, v99, v2
	v_add_u32_e32 v4, v118, v4
	s_add_u32 s2, s2, 0x1000
	v_ashrrev_i32_e32 v93, 5, v2
	v_and_b32_e32 v2, 0xffffffe0, v2
	v_ashrrev_i32_e32 v100, 5, v4
	v_and_b32_e32 v4, 0xffffffe0, v4
	v_add_u32_e32 v119, 0x400, v99
	v_add_u32_e32 v120, 0x600, v99
	s_addc_u32 s3, s3, 0
	v_sub_u32_e32 v92, v99, v2
	v_sub_u32_e32 v94, v118, v4
	v_ashrrev_i32_e32 v126, 31, v119
	v_ashrrev_i32_e32 v128, 31, v120
	v_mov_b64_e32 v[30:31], s[2:3]
	v_lshlrev_b32_e32 v74, 3, v92
	v_lshlrev_b32_e32 v76, 3, v94
	v_lshrrev_b32_e32 v10, 27, v126
	v_lshrrev_b32_e32 v12, 27, v128
	v_mad_i64_i32 v[2:3], s[2:3], v93, s68, v[30:31]
	v_ashrrev_i32_e32 v75, 31, v74
	v_mad_i64_i32 v[4:5], s[2:3], v100, s68, v[30:31]
	v_ashrrev_i32_e32 v77, 31, v76
	v_add_u32_e32 v10, v119, v10
	v_add_u32_e32 v12, v120, v12
	v_lshl_add_u64 v[2:3], v[74:75], 1, v[2:3]
	v_lshl_add_u64 v[6:7], v[76:77], 1, v[4:5]
	v_ashrrev_i32_e32 v101, 5, v10
	v_and_b32_e32 v10, 0xffffffe0, v10
	v_ashrrev_i32_e32 v102, 5, v12
	v_and_b32_e32 v12, 0xffffffe0, v12
	v_add_u32_e32 v123, 0x800, v99
	v_add_u32_e32 v125, 0xa00, v99
	v_add_u32_e32 v127, 0xc00, v99
	v_add_u32_e32 v129, 0xe00, v99
	global_load_dwordx4 v[2:5], v[2:3], off
	s_nop 0
	global_load_dwordx4 v[6:9], v[6:7], off
	v_sub_u32_e32 v98, v119, v10
	v_sub_u32_e32 v110, v120, v12
	v_ashrrev_i32_e32 v130, 31, v123
	v_ashrrev_i32_e32 v131, 31, v125
	v_ashrrev_i32_e32 v132, 31, v127
	v_ashrrev_i32_e32 v133, 31, v129
	v_lshlrev_b32_e32 v78, 3, v98
	v_lshlrev_b32_e32 v80, 3, v110
	v_lshrrev_b32_e32 v18, 27, v130
	v_lshrrev_b32_e32 v20, 27, v131
	v_lshrrev_b32_e32 v26, 27, v132
	v_lshrrev_b32_e32 v32, 27, v133
	v_and_b32_e32 v71, 15, v99
	v_mad_i64_i32 v[10:11], s[2:3], v101, s68, v[30:31]
	v_ashrrev_i32_e32 v79, 31, v78
	v_mad_i64_i32 v[12:13], s[2:3], v102, s68, v[30:31]
	v_ashrrev_i32_e32 v81, 31, v80
	v_add_u32_e32 v18, v123, v18
	v_add_u32_e32 v20, v125, v20
	v_add_u32_e32 v26, v127, v26
	v_add_u32_e32 v32, v129, v32
	v_lshl_add_u64 v[10:11], v[78:79], 1, v[10:11]
	v_lshl_add_u64 v[14:15], v[80:81], 1, v[12:13]
	v_ashrrev_i32_e32 v103, 5, v18
	v_and_b32_e32 v18, 0xffffffe0, v18
	v_ashrrev_i32_e32 v104, 5, v20
	v_and_b32_e32 v20, 0xffffffe0, v20
	v_ashrrev_i32_e32 v105, 5, v26
	v_and_b32_e32 v26, 0xffffffe0, v26
	v_ashrrev_i32_e32 v106, 5, v32
	v_and_b32_e32 v32, 0xffffffe0, v32
	v_lshl_or_b32 v135, s23, 4, v71
	global_load_dwordx4 v[10:13], v[10:11], off
	s_nop 0
	global_load_dwordx4 v[14:17], v[14:15], off
	v_sub_u32_e32 v111, v123, v18
	v_sub_u32_e32 v112, v125, v20
	v_sub_u32_e32 v113, v127, v26
	v_sub_u32_e32 v114, v129, v32
	v_add_u32_e32 v70, s14, v135
	v_lshlrev_b32_e32 v82, 3, v111
	v_lshlrev_b32_e32 v84, 3, v112
	v_lshlrev_b32_e32 v86, 3, v113
	v_lshlrev_b32_e32 v88, 3, v114
	v_mad_i64_i32 v[72:73], s[2:3], v70, s68, v[68:69]
	v_mad_i64_i32 v[18:19], s[2:3], v103, s68, v[30:31]
	v_ashrrev_i32_e32 v83, 31, v82
	v_mad_i64_i32 v[20:21], s[2:3], v104, s68, v[30:31]
	v_ashrrev_i32_e32 v85, 31, v84
	v_mad_i64_i32 v[26:27], s[2:3], v105, s68, v[30:31]
	v_ashrrev_i32_e32 v87, 31, v86
	v_mad_i64_i32 v[30:31], s[2:3], v106, s68, v[30:31]
	v_ashrrev_i32_e32 v89, 31, v88
	v_lshl_add_u64 v[34:35], v[72:73], 0, s[24:25]
	v_and_b32_e32 v66, 48, v99
	v_lshl_add_u64 v[18:19], v[82:83], 1, v[18:19]
	v_lshl_add_u64 v[22:23], v[84:85], 1, v[20:21]
	v_lshl_add_u64 v[26:27], v[86:87], 1, v[26:27]
	v_lshl_add_u64 v[30:31], v[88:89], 1, v[30:31]
	v_lshl_add_u64 v[90:91], v[34:35], 0, v[66:67]
	global_load_dwordx4 v[18:21], v[18:19], off
	s_nop 0
	global_load_dwordx4 v[22:25], v[22:23], off
	v_mul_lo_u32 v108, v93, s69
	global_load_dwordx4 v[26:29], v[26:27], off
	v_lshlrev_b32_e32 v107, 4, v92
	global_load_dwordx4 v[30:33], v[30:31], off
	s_nop 0
	global_load_dwordx4 v[62:65], v[90:91], off offset:2048
	global_load_dwordx4 v[58:61], v[90:91], off offset:2112
	global_load_dwordx4 v[54:57], v[90:91], off offset:2176
	global_load_dwordx4 v[50:53], v[90:91], off offset:2240
	global_load_dwordx4 v[46:49], v[90:91], off offset:2304
	global_load_dwordx4 v[42:45], v[90:91], off offset:2368
	global_load_dwordx4 v[38:41], v[90:91], off offset:2432
	global_load_dwordx4 v[34:37], v[90:91], off offset:2496
	v_mov_b32_e32 v245, 0
	v_cmp_gt_i32_e32 vcc, s64, v99
	v_cmp_lt_i32_e64 s[2:3], s65, v99
	s_barrier
	s_and_saveexec_b64 s[4:5], s[2:3]
	s_xor_b64 s[4:5], exec, s[4:5]
	s_cbranch_execz .LBB0_562
	v_cmp_gt_u32_e64 s[2:3], s67, v99
	s_and_saveexec_b64 s[6:7], s[2:3]
	s_cbranch_execz .LBB0_561
	s_ashr_i32 s23, s22, 31
	s_lshl_b64 s[2:3], s[22:23], 10
	s_add_u32 s2, s58, s2
	v_add_u32_e32 v244, 0xffffff80, v99
	s_addc_u32 s3, s59, s3
	v_lshl_add_u64 v[240:241], v[244:245], 2, s[2:3]
	global_load_dword v240, v[240:241], off
	v_lshl_add_u32 v241, v99, 2, s62
	s_waitcnt vmcnt(0)
	ds_write_b32 v241, v240

; #define MFMA16(b, a, c) __builtin_amdgcn_mfma_f32_16x16x32_bf16((b), (a), (c), 0, 0, 0)
; __device__ __forceinline__ void mlstm_D(LAS unsigned char* lds, int c, int h, const bf16_t* Z, const float* gi, const float* bcum, const float* marr, const bf16_t* CST, const float* NST,
;                                         const float* hgain, bf16_t* YCAT) {
;     ...
;     const int t0 = c * CH; const float mc = marr[h * 65 + c];
;     __syncthreads();
;     if (tid < CH) gS[tid] = gi[(size_t)(t0 + tid) * 4 + h];
;     else if (tid < CH + DH) nst[tid - CH] = NST[(size_t)(c * NH + h) * DH + (tid - CH)];
;     __syncthreads();
;     if (tid < CH) { float m = mc; for (int s = 0; s <= tid; ++s) m = fmaxf(m, gS[s]); Mrow[tid] = m; }
;     stage_tile<CH, DH, 8>(X, Z + (size_t)t0 * EVN + 2048 + h * DH, EVN, tid);
;     const int tl = 16 * wave + fr; const size_t trow = (size_t)(t0 + tl);
;     bf16x8 aq[8];
; #pragma unroll
;     for (int ks = 0; ks < 8; ++ks) aq[ks] = *(const bf16x8*)(Z + trow * EVN + 1024 + h * DH + 32 * ks + 8 * fq);
;     __syncthreads();
;     f32x4 S[8];
; #pragma unroll
;     for (int j = 0; j < 8; ++j) S[j] = (f32x4){0.f, 0.f, 0.f, 0.f};
; #pragma unroll
;     for (int ks = 0; ks < 8; ++ks)
;         {
; #pragma unroll
;           for (int j = 0; j < 8; ++j) if (j <= wave) S[j] = MFMA16(row_frag(X, (DH + 8) * 2, 16 * j, 32 * ks, lane), aq[ks], S[j]);
.LBB0_562:
	s_or_saveexec_b64 s[2:3], s[4:5]
	s_lshl_b32 s14, s8, 7
	s_xor_b64 exec, exec, s[2:3]
	s_cbranch_execz .LBB0_564
	v_add_u32_e32 v240, s14, v99
	v_ashrrev_i32_e32 v241, 31, v240
	v_lshl_add_u64 v[240:241], v[240:241], 4, s[42:43]
	s_lshl_b32 s24, s36, 2
	v_lshl_add_u64 v[240:241], v[240:241], 0, s[24:25]
	global_load_dword v240, v[240:241], off
	v_lshl_add_u32 v241, v99, 2, s61
	s_waitcnt vmcnt(0)
	ds_write_b32 v241, v240
.LBB0_564:
	s_or_b64 exec, exec, s[2:3]
	s_waitcnt lgkmcnt(0)
	s_barrier
	s_and_saveexec_b64 s[4:5], vcc
	s_cbranch_execz .LBB0_576
	v_and_b32_e32 v241, 63, v99
	v_lshl_add_u32 v240, v99, 2, s61
	v_lshl_add_u32 v241, v241, 2, s61
	ds_read_b32 v242, v240
	ds_read_b32 v243, v241
	s_waitcnt vmcnt(0) lgkmcnt(0)
	s_nop 1
	v_max_f32_dpp v242, v242, v242 row_shr:1 row_mask:0xf bank_mask:0xf
	v_max_f32_dpp v243, v243, v243 row_shr:1 row_mask:0xf bank_mask:0xf
	s_nop 1
	v_max_f32_dpp v242, v242, v242 row_shr:2 row_mask:0xf bank_mask:0xf
	v_max_f32_dpp v243, v243, v243 row_shr:2 row_mask:0xf bank_mask:0xf
	s_nop 1
	v_max_f32_dpp v242, v242, v242 row_shr:4 row_mask:0xf bank_mask:0xf
	v_max_f32_dpp v243, v243, v243 row_shr:4 row_mask:0xf bank_mask:0xf
	s_nop 1
	v_max_f32_dpp v242, v242, v242 row_shr:8 row_mask:0xf bank_mask:0xf
	v_max_f32_dpp v243, v243, v243 row_shr:8 row_mask:0xf bank_mask:0xf
	s_nop 1
	v_max_f32_dpp v242, v242, v242 row_bcast:15 row_mask:0xa bank_mask:0xf
	v_max_f32_dpp v243, v243, v243 row_bcast:15 row_mask:0xa bank_mask:0xf
	s_nop 1
	v_max_f32_dpp v242, v242, v242 row_bcast:31 row_mask:0xc bank_mask:0xf
	v_max_f32_dpp v243, v243, v243 row_bcast:31 row_mask:0xc bank_mask:0xf
	s_nop 1
	v_readlane_b32 s2, v243, 63
	v_readfirstlane_b32 s3, v95
	s_cmp_ge_u32 s15, 64
	s_cselect_b32 s2, s2, s3
	v_max_f32_e32 v242, s2, v242
	v_max_f32_e32 v242, v95, v242
	v_lshl_add_u32 v240, v99, 2, s62
	ds_write_b32 v240, v242
.LBB0_576:
	s_or_b64 exec, exec, s[4:5]
	s_ashr_i32 s23, s15, 6
	v_add3_u32 v92, s51, v108, v107
	v_lshlrev_b32_e32 v108, 4, v94
	v_lshlrev_b32_e32 v109, 4, v98
	v_lshlrev_b32_e32 v110, 4, v110
	v_lshlrev_b32_e32 v111, 4, v111
	v_lshlrev_b32_e32 v112, 4, v112
	v_lshlrev_b32_e32 v113, 4, v113
	s_waitcnt vmcnt(15)
	ds_write_b128 v92, v[2:5]
	v_mul_lo_u32 v2, v100, s69
	v_add3_u32 v2, s51, v2, v108
	s_waitcnt vmcnt(14)
	ds_write_b128 v2, v[6:9]
	v_mul_lo_u32 v2, v101, s69
	v_add3_u32 v2, s51, v2, v109
	v_lshlrev_b32_e32 v114, 4, v114
	v_add_u32_e32 v121, s51, v66
	s_cmp_gt_i32 s23, -1
	s_cselect_b64 s[4:5], -1, 0
	s_cmp_lt_i32 s23, 0
	v_mad_u32_u24 v92, v71, s69, v121
	s_waitcnt vmcnt(13)
	ds_write_b128 v2, v[10:13]
	v_mul_lo_u32 v2, v102, s69
	v_add3_u32 v2, s51, v2, v110
	s_waitcnt vmcnt(12)
	ds_write_b128 v2, v[14:17]
	v_mul_lo_u32 v2, v103, s69
	v_add3_u32 v2, s51, v2, v111
	s_waitcnt vmcnt(11)
	ds_write_b128 v2, v[18:21]
	v_mul_lo_u32 v2, v104, s69
	v_add3_u32 v2, s51, v2, v112
	s_waitcnt vmcnt(10)
	ds_write_b128 v2, v[22:25]
	v_mul_lo_u32 v2, v105, s69
	v_add3_u32 v2, s51, v2, v113
	s_waitcnt vmcnt(9)
	ds_write_b128 v2, v[26:29]
	v_mul_lo_u32 v2, v106, s69
	v_add3_u32 v2, s51, v2, v114
	s_waitcnt vmcnt(8)
	ds_write_b128 v2, v[30:33]
	v_mov_b32_e32 v30, v67
	v_mov_b32_e32 v31, v67
	v_mov_b32_e32 v32, v67
	v_mov_b32_e32 v33, v67
	s_waitcnt lgkmcnt(0)
	s_barrier
	ds_read_b128 v[136:139], v92
	ds_read_b128 v[140:143], v92 offset:8448
	ds_read_b128 v[144:147], v92 offset:16896
	ds_read_b128 v[148:151], v92 offset:25344
	ds_read_b128 v[152:155], v92 offset:33792
	ds_read_b128 v[156:159], v92 offset:42240
	ds_read_b128 v[160:163], v92 offset:50688
	ds_read_b128 v[164:167], v92 offset:59136
	ds_read_b128 v[168:171], v92 offset:64
	ds_read_b128 v[172:175], v92 offset:8512
	ds_read_b128 v[176:179], v92 offset:16960
	ds_read_b128 v[180:183], v92 offset:25408
	ds_read_b128 v[184:187], v92 offset:33856
	ds_read_b128 v[188:191], v92 offset:42304
	ds_read_b128 v[192:195], v92 offset:50752
	ds_read_b128 v[196:199], v92 offset:59200
	s_waitcnt vmcnt(7) lgkmcnt(8)
	v_mfma_f32_16x16x32_bf16 v[30:33], v[136:139], v[62:65], 0
	v_mfma_f32_16x16x32_bf16 v[26:29], v[140:143], v[62:65], 0
	v_mfma_f32_16x16x32_bf16 v[22:25], v[144:147], v[62:65], 0
	v_mfma_f32_16x16x32_bf16 v[18:21], v[148:151], v[62:65], 0
	v_mfma_f32_16x16x32_bf16 v[14:17], v[152:155], v[62:65], 0
	v_mfma_f32_16x16x32_bf16 v[10:13], v[156:159], v[62:65], 0
	v_mfma_f32_16x16x32_bf16 v[6:9], v[160:163], v[62:65], 0
	v_mfma_f32_16x16x32_bf16 v[2:5], v[164:167], v[62:65], 0
	ds_read_b128 v[136:139], v92 offset:128
	ds_read_b128 v[140:143], v92 offset:8576
	ds_read_b128 v[144:147], v92 offset:17024
	ds_read_b128 v[148:151], v92 offset:25472
	ds_read_b128 v[152:155], v92 offset:33920
	ds_read_b128 v[156:159], v92 offset:42368
	ds_read_b128 v[160:163], v92 offset:50816
	ds_read_b128 v[164:167], v92 offset:59264
	s_waitcnt vmcnt(6) lgkmcnt(8)
; #define MFMA16(b, a, c) __builtin_amdgcn_mfma_f32_16x16x32_bf16((b), (a), (c), 0, 0, 0)
; __device__ __forceinline__ void mlstm_D(LAS unsigned char* lds, int c, int h, const bf16_t* Z, const float* gi, const float* bcum, const float* marr, const bf16_t* CST, const float* NST,
;                                         const float* hgain, bf16_t* YCAT) {
;     ...
; #pragma unroll
;     for (int ks = 0; ks < 8; ++ks)
;         {
; #pragma unroll
;           for (int j = 0; j < 8; ++j) if (j <= wave) S[j] = MFMA16(row_frag(X, (DH + 8) * 2, 16 * j, 32 * ks, lane), aq[ks], S[j]);
;           asm volatile("" ::: "memory"); }
	v_mfma_f32_16x16x32_bf16 v[30:33], v[168:171], v[58:61], v[30:33]
	v_mfma_f32_16x16x32_bf16 v[26:29], v[172:175], v[58:61], v[26:29]
	v_mfma_f32_16x16x32_bf16 v[22:25], v[176:179], v[58:61], v[22:25]
	v_mfma_f32_16x16x32_bf16 v[18:21], v[180:183], v[58:61], v[18:21]
	v_mfma_f32_16x16x32_bf16 v[14:17], v[184:187], v[58:61], v[14:17]
	v_mfma_f32_16x16x32_bf16 v[10:13], v[188:191], v[58:61], v[10:13]
	v_mfma_f32_16x16x32_bf16 v[6:9], v[192:195], v[58:61], v[6:9]
	v_mfma_f32_16x16x32_bf16 v[2:5], v[196:199], v[58:61], v[2:5]
	ds_read_b128 v[168:171], v92 offset:192
	ds_read_b128 v[172:175], v92 offset:8640
	ds_read_b128 v[176:179], v92 offset:17088
	ds_read_b128 v[180:183], v92 offset:25536
	ds_read_b128 v[184:187], v92 offset:33984
	ds_read_b128 v[188:191], v92 offset:42432
	ds_read_b128 v[192:195], v92 offset:50880
	ds_read_b128 v[196:199], v92 offset:59328
	s_waitcnt vmcnt(5) lgkmcnt(8)
	v_mfma_f32_16x16x32_bf16 v[30:33], v[136:139], v[54:57], v[30:33]
	v_mfma_f32_16x16x32_bf16 v[26:29], v[140:143], v[54:57], v[26:29]
	v_mfma_f32_16x16x32_bf16 v[22:25], v[144:147], v[54:57], v[22:25]
	v_mfma_f32_16x16x32_bf16 v[18:21], v[148:151], v[54:57], v[18:21]
	v_mfma_f32_16x16x32_bf16 v[14:17], v[152:155], v[54:57], v[14:17]
	v_mfma_f32_16x16x32_bf16 v[10:13], v[156:159], v[54:57], v[10:13]
	v_mfma_f32_16x16x32_bf16 v[6:9], v[160:163], v[54:57], v[6:9]
	v_mfma_f32_16x16x32_bf16 v[2:5], v[164:167], v[54:57], v[2:5]
	ds_read_b128 v[136:139], v92 offset:256
	ds_read_b128 v[140:143], v92 offset:8704
	ds_read_b128 v[144:147], v92 offset:17152
	ds_read_b128 v[148:151], v92 offset:25600
	ds_read_b128 v[152:155], v92 offset:34048
	ds_read_b128 v[156:159], v92 offset:42496
	ds_read_b128 v[160:163], v92 offset:50944
	ds_read_b128 v[164:167], v92 offset:59392
	s_waitcnt vmcnt(4) lgkmcnt(8)
	v_mfma_f32_16x16x32_bf16 v[30:33], v[168:171], v[50:53], v[30:33]
	v_mfma_f32_16x16x32_bf16 v[26:29], v[172:175], v[50:53], v[26:29]
	v_mfma_f32_16x16x32_bf16 v[22:25], v[176:179], v[50:53], v[22:25]
	v_mfma_f32_16x16x32_bf16 v[18:21], v[180:183], v[50:53], v[18:21]
	v_mfma_f32_16x16x32_bf16 v[14:17], v[184:187], v[50:53], v[14:17]
	v_mfma_f32_16x16x32_bf16 v[10:13], v[188:191], v[50:53], v[10:13]
	v_mfma_f32_16x16x32_bf16 v[6:9], v[192:195], v[50:53], v[6:9]
	v_mfma_f32_16x16x32_bf16 v[2:5], v[196:199], v[50:53], v[2:5]
	ds_read_b128 v[168:171], v92 offset:320
	ds_read_b128 v[172:175], v92 offset:8768
	ds_read_b128 v[176:179], v92 offset:17216
	ds_read_b128 v[180:183], v92 offset:25664
	ds_read_b128 v[184:187], v92 offset:34112
	ds_read_b128 v[188:191], v92 offset:42560
	ds_read_b128 v[192:195], v92 offset:51008
	ds_read_b128 v[196:199], v92 offset:59456
	s_waitcnt vmcnt(3) lgkmcnt(8)
	v_mfma_f32_16x16x32_bf16 v[30:33], v[136:139], v[46:49], v[30:33]
	v_mfma_f32_16x16x32_bf16 v[26:29], v[140:143], v[46:49], v[26:29]
	v_mfma_f32_16x16x32_bf16 v[22:25], v[144:147], v[46:49], v[22:25]
	v_mfma_f32_16x16x32_bf16 v[18:21], v[148:151], v[46:49], v[18:21]
	v_mfma_f32_16x16x32_bf16 v[14:17], v[152:155], v[46:49], v[14:17]
	v_mfma_f32_16x16x32_bf16 v[10:13], v[156:159], v[46:49], v[10:13]
	v_mfma_f32_16x16x32_bf16 v[6:9], v[160:163], v[46:49], v[6:9]
	v_mfma_f32_16x16x32_bf16 v[2:5], v[164:167], v[46:49], v[2:5]
	ds_read_b128 v[136:139], v92 offset:384
	ds_read_b128 v[140:143], v92 offset:8832
	ds_read_b128 v[144:147], v92 offset:17280
	ds_read_b128 v[148:151], v92 offset:25728
	ds_read_b128 v[152:155], v92 offset:34176
	ds_read_b128 v[156:159], v92 offset:42624
	ds_read_b128 v[160:163], v92 offset:51072
	ds_read_b128 v[164:167], v92 offset:59520
	s_waitcnt vmcnt(2) lgkmcnt(8)
	v_mfma_f32_16x16x32_bf16 v[30:33], v[168:171], v[42:45], v[30:33]
	v_mfma_f32_16x16x32_bf16 v[26:29], v[172:175], v[42:45], v[26:29]
	v_mfma_f32_16x16x32_bf16 v[22:25], v[176:179], v[42:45], v[22:25]
	v_mfma_f32_16x16x32_bf16 v[18:21], v[180:183], v[42:45], v[18:21]
	v_mfma_f32_16x16x32_bf16 v[14:17], v[184:187], v[42:45], v[14:17]
	v_mfma_f32_16x16x32_bf16 v[10:13], v[188:191], v[42:45], v[10:13]
	v_mfma_f32_16x16x32_bf16 v[6:9], v[192:195], v[42:45], v[6:9]
	v_mfma_f32_16x16x32_bf16 v[2:5], v[196:199], v[42:45], v[2:5]
	ds_read_b128 v[168:171], v92 offset:448
	ds_read_b128 v[172:175], v92 offset:8896
	ds_read_b128 v[176:179], v92 offset:17344
	ds_read_b128 v[180:183], v92 offset:25792
	ds_read_b128 v[184:187], v92 offset:34240
	ds_read_b128 v[188:191], v92 offset:42688
	ds_read_b128 v[192:195], v92 offset:51136
	ds_read_b128 v[196:199], v92 offset:59584
	s_waitcnt vmcnt(1) lgkmcnt(8)
	v_mfma_f32_16x16x32_bf16 v[30:33], v[136:139], v[38:41], v[30:33]
	v_mfma_f32_16x16x32_bf16 v[26:29], v[140:143], v[38:41], v[26:29]
	v_mfma_f32_16x16x32_bf16 v[22:25], v[144:147], v[38:41], v[22:25]
	v_mfma_f32_16x16x32_bf16 v[18:21], v[148:151], v[38:41], v[18:21]
	v_mfma_f32_16x16x32_bf16 v[14:17], v[152:155], v[38:41], v[14:17]
	v_mfma_f32_16x16x32_bf16 v[10:13], v[156:159], v[38:41], v[10:13]
	v_mfma_f32_16x16x32_bf16 v[6:9], v[160:163], v[38:41], v[6:9]
	v_mfma_f32_16x16x32_bf16 v[2:5], v[164:167], v[38:41], v[2:5]
	s_waitcnt vmcnt(0) lgkmcnt(0)
	v_mfma_f32_16x16x32_bf16 v[30:33], v[168:171], v[34:37], v[30:33]
	v_mfma_f32_16x16x32_bf16 v[26:29], v[172:175], v[34:37], v[26:29]
	v_mfma_f32_16x16x32_bf16 v[22:25], v[176:179], v[34:37], v[22:25]
	v_mfma_f32_16x16x32_bf16 v[18:21], v[180:183], v[34:37], v[18:21]
	v_mfma_f32_16x16x32_bf16 v[14:17], v[184:187], v[34:37], v[14:17]
	v_mfma_f32_16x16x32_bf16 v[10:13], v[188:191], v[34:37], v[10:13]
	v_mfma_f32_16x16x32_bf16 v[6:9], v[192:195], v[34:37], v[6:9]
	v_mfma_f32_16x16x32_bf16 v[2:5], v[196:199], v[34:37], v[2:5]
